# out-projection epilogue: gate vectors and first residual rows loaded together (one round trip instead of three before the first row block)
# speedup vs baseline: 1.0718x; 1.0718x over previous
.LBB0_705:
	s_lshl_b32 s0, s42, 8
	v_mov_b32_e32 v14, v3
	v_mov_b32_e32 v15, v170
	s_add_i32 s0, s0, s36
	s_nop 15
	s_nop 15
	s_nop 0
	v_add_u32_e32 v198, s0, v14
	s_lshl_b32 s0, s33, 8
	s_or_b32 s0, s0, s37
	v_lshl_add_u32 v32, v15, 3, s0
	s_lshr_b32 s0, s42, 6
	s_mulk_i32 s0, 0x1800
	s_ashr_i32 s1, s0, 31
	s_lshl_b64 s[0:1], s[0:1], 2
	s_add_u32 s0, s31, s0
	s_addc_u32 s1, s34, s1
	v_ashrrev_i32_e32 v33, 31, v32
	v_lshl_add_u64 v[12:13], v[32:33], 2, s[0:1]
	global_load_dwordx4 v[4:7], v[12:13], off offset:16
	global_load_dwordx4 v[8:11], v[12:13], off
	global_load_dwordx4 v[212:215], v[12:13], off offset:528
	global_load_dwordx4 v[216:219], v[12:13], off offset:512
	s_mov_b32 s0, 0x3b000000
	v_lshlrev_b64 v[208:209], 1, v[32:33]
	v_ashrrev_i32_e32 v199, 31, v198
	v_lshl_add_u64 v[200:201], s[6:7], 0, v[208:209]
	v_add_u32_e32 v206, 16, v198
	v_ashrrev_i32_e32 v207, 31, v206
	v_add_u32_e32 v204, 32, v198
	v_ashrrev_i32_e32 v205, 31, v204
	v_add_u32_e32 v202, 48, v198
	v_ashrrev_i32_e32 v203, 31, v202
	v_cmp_eq_u32_e32 vcc, 0, v15
	v_lshlrev_b32_e32 v220, 2, v14
	v_lshl_add_u32 v220, v15, 6, v220
	v_xor_b32_e32 v229, 64, v220
	v_xor_b32_e32 v228, 0x80, v220
	v_lshlrev_b64 v[220:221], 11, v[198:199]
	v_lshl_add_u64 v[220:221], v[200:201], 0, v[220:221]
	global_load_dwordx4 v[230:233], v[220:221], off
	global_load_dwordx4 v[28:31], v[220:221], off offset:256
	v_lshlrev_b64 v[220:221], 11, v[206:207]
	v_lshl_add_u64 v[220:221], v[200:201], 0, v[220:221]
	global_load_dwordx4 v[24:27], v[220:221], off
	global_load_dwordx4 v[20:23], v[220:221], off offset:256
	v_lshlrev_b64 v[220:221], 11, v[204:205]
	v_lshl_add_u64 v[220:221], v[200:201], 0, v[220:221]
	global_load_dwordx4 v[16:19], v[220:221], off
	global_load_dwordx4 v[12:15], v[220:221], off offset:256
	v_lshlrev_b64 v[220:221], 11, v[202:203]
	v_lshl_add_u64 v[220:221], v[200:201], 0, v[220:221]
	s_waitcnt vmcnt(8)
	v_pk_mul_f32 v[192:193], v[6:7], s[0:1] op_sel_hi:[1,0]
	v_pk_mul_f32 v[196:197], v[10:11], s[0:1] op_sel_hi:[1,0]
	v_pk_mul_f32 v[194:195], v[8:9], s[0:1] op_sel_hi:[1,0]
	v_pk_mul_f32 v[190:191], v[4:5], s[0:1] op_sel_hi:[1,0]
	s_waitcnt vmcnt(6)
	v_pk_mul_f32 v[34:35], v[212:213], s[0:1] op_sel_hi:[1,0]
	v_pk_mul_f32 v[188:189], v[218:219], s[0:1] op_sel_hi:[1,0]
	v_pk_mul_f32 v[186:187], v[216:217], s[0:1] op_sel_hi:[1,0]
	v_pk_mul_f32 v[184:185], v[214:215], s[0:1] op_sel_hi:[1,0]
	global_load_dwordx4 v[8:11], v[220:221], off
	s_nop 0
	global_load_dwordx4 v[4:7], v[220:221], off offset:256
	v_mov_b32_e32 v212, 0x3b808081
	v_mov_b32_e32 v213, 0x398637bd
	v_mov_b32_e32 v214, 0x7f800000
	v_mov_b32_e32 v215, 0x7fc00000
	v_mov_b32_e32 v216, 0xff800000
	v_mov_b32_e32 v217, 0xff61b1e6
	v_mov_b32_e32 v218, 0x3f80
	v_mov_b32_e32 v219, 0x4800
	v_bfrev_b32_e32 v220, 0.5
	v_mov_b32_e32 v221, 0x3fb8aa3b
	s_lshl_b32 s0, s33, 2
	s_ashr_i32 s1, s0, 31
	s_waitcnt vmcnt(7)
	v_lshlrev_b32_e32 v164, 16, v230
	v_and_b32_e32 v165, 0xffff0000, v230
	v_lshlrev_b32_e32 v166, 16, v231
	v_and_b32_e32 v167, 0xffff0000, v231
	v_pk_fma_f32 v[166:167], v[162:163], v[196:197], v[166:167]
	v_pk_fma_f32 v[164:165], v[160:161], v[194:195], v[164:165]
	v_lshlrev_b32_e32 v160, 16, v232
	v_and_b32_e32 v161, 0xffff0000, v232
	v_lshlrev_b32_e32 v162, 16, v233
	v_and_b32_e32 v163, 0xffff0000, v233
	v_pk_fma_f32 v[158:159], v[158:159], v[192:193], v[162:163]
	v_pk_fma_f32 v[156:157], v[156:157], v[190:191], v[160:161]
	v_cvt_pk_bf16_f32 v160, v164, v165
	v_cvt_pk_bf16_f32 v161, v166, v167
	v_cvt_pk_bf16_f32 v162, v156, v157
	v_cvt_pk_bf16_f32 v163, v158, v159
	v_pk_mul_f32 v[166:167], v[166:167], v[166:167]
	v_pk_mul_f32 v[164:165], v[164:165], v[164:165]
	v_pk_mul_f32 v[158:159], v[158:159], v[158:159]
	v_pk_mul_f32 v[156:157], v[156:157], v[156:157]
	v_add_f32_e32 v164, v164, v165
	v_add_f32_e32 v165, v166, v167
	v_add_f32_e32 v156, v156, v157
	v_add_f32_e32 v157, v158, v159
	v_add_f32_e32 v164, v164, v165
	v_add_f32_e32 v156, v156, v157
	v_add_f32_e32 v158, v164, v156
	v_lshlrev_b32_e32 v156, 11, v198
	v_and_b32_e32 v156, 0x3fff800, v156
	v_mov_b32_e32 v157, v2
	v_lshl_add_u64 v[156:157], s[6:7], 0, v[156:157]
	v_lshl_add_u64 v[156:157], v[156:157], 0, v[208:209]
	global_store_dwordx4 v[156:157], v[160:163], off
	s_waitcnt vmcnt(7)
	s_nop 0
	v_lshlrev_b32_e32 v160, 16, v28
	v_and_b32_e32 v161, 0xffff0000, v28
	v_lshlrev_b32_e32 v28, 16, v29
	v_and_b32_e32 v29, 0xffff0000, v29
	v_pk_fma_f32 v[154:155], v[154:155], v[188:189], v[28:29]
	v_lshlrev_b32_e32 v28, 16, v30
	v_and_b32_e32 v29, 0xffff0000, v30
	v_lshlrev_b32_e32 v30, 16, v31
	v_and_b32_e32 v31, 0xffff0000, v31
	v_pk_fma_f32 v[152:153], v[152:153], v[186:187], v[160:161]
	v_pk_fma_f32 v[150:151], v[150:151], v[184:185], v[30:31]
	v_pk_fma_f32 v[148:149], v[148:149], v[34:35], v[28:29]
	v_cvt_pk_bf16_f32 v28, v152, v153
	v_cvt_pk_bf16_f32 v29, v154, v155
	v_cvt_pk_bf16_f32 v30, v148, v149
	v_cvt_pk_bf16_f32 v31, v150, v151
	v_pk_mul_f32 v[154:155], v[154:155], v[154:155]
	v_pk_mul_f32 v[152:153], v[152:153], v[152:153]
	v_pk_mul_f32 v[150:151], v[150:151], v[150:151]
	v_pk_mul_f32 v[148:149], v[148:149], v[148:149]
	v_add_f32_e32 v152, v152, v153
	v_add_f32_e32 v153, v154, v155
	v_add_f32_e32 v148, v148, v149
	v_add_f32_e32 v149, v150, v151
	v_add_f32_e32 v152, v152, v153
	v_add_f32_e32 v148, v148, v149
	v_add_f32_e32 v148, v152, v148
	v_add_f32_e32 v148, v158, v148
	global_store_dwordx4 v[156:157], v[28:31], off offset:256
	ds_bpermute_b32 v28, v229, v148
	s_waitcnt lgkmcnt(0)
	v_add_f32_e32 v28, v148, v28
	ds_bpermute_b32 v29, v228, v28
	s_and_saveexec_b64 s[18:19], vcc
	s_mov_b32 s53, s49
	v_readlane_b32 s46, v252, 58
	s_cbranch_execz .LBB0_707
	v_lshlrev_b64 v[30:31], 6, v[198:199]
	v_lshl_add_u64 v[30:31], s[8:9], 0, v[30:31]
	v_lshl_add_u64 v[30:31], s[0:1], 2, v[30:31]
	s_lshl_b32 s52, s35, 2
	v_lshl_add_u64 v[30:31], v[30:31], 0, s[52:53]
	s_waitcnt lgkmcnt(0)
	v_add_f32_e32 v28, v28, v29
	global_store_dword v[30:31], v28, off
